# speedup vs baseline: 1.1984x; 1.0148x over previous
.Lk_328:
	s_or_b64 exec, exec, s[0:1]
	s_waitcnt lgkmcnt(0)
	s_barrier
	s_and_saveexec_b64 s[4:5], s[42:43]
	s_cbranch_execz .Lk_388
	v_cvt_f32_f64_e32 v3, v[38:39]
	v_cvt_f32_f64_e32 v2, v[36:37]
	v_cvt_f32_f64_e32 v6, v[6:7]
	v_cvt_f32_f64_e32 v4, v[4:5]
	ds_read_b32 v100, v67
	ds_read_b32 v110, v69
	ds_read_b32 v101, v67 offset:2048
	ds_read_b32 v111, v69 offset:2048
	ds_read_b32 v102, v67 offset:4096
	ds_read_b32 v112, v69 offset:4096
	ds_read_b32 v103, v67 offset:6144
	ds_read_b32 v113, v69 offset:6144
	ds_read_b32 v104, v67 offset:8192
	ds_read_b32 v114, v69 offset:8192
	ds_read_b32 v105, v67 offset:10240
	ds_read_b32 v115, v69 offset:10240
	ds_read_b32 v106, v67 offset:12288
	ds_read_b32 v116, v69 offset:12288
	ds_read_b32 v107, v67 offset:14336
	ds_read_b32 v117, v69 offset:14336
	ds_read_b32 v108, v67 offset:16384
	ds_read_b32 v118, v69 offset:16384
	ds_read_b32 v109, v67 offset:18432
	ds_read_b32 v119, v69 offset:18432
	v_lshrrev_b32_e32 v0, 5, v160
	v_mov_b32_e32 v1, 0x25000
	v_lshl_or_b32 v1, v0, 2, v1
	s_mov_b32 s6, 0x80000000
	s_mov_b32 s7, 0x80000000
	s_waitcnt lgkmcnt(0)
	v_mul_f32_e32 v120, v110, v3
	v_mul_f32_e32 v121, v111, v3
	v_mul_f32_e32 v122, v112, v3
	v_mul_f32_e32 v123, v113, v3
	v_mul_f32_e32 v124, v114, v3
	v_mul_f32_e32 v125, v115, v3
	v_mul_f32_e32 v126, v116, v3
	v_mul_f32_e32 v127, v117, v3
	v_mul_f32_e32 v128, v118, v3
	v_mul_f32_e32 v129, v119, v3
	v_fmac_f32_e32 v120, v100, v2
	v_fmac_f32_e32 v121, v101, v2
	v_fmac_f32_e32 v122, v102, v2
	v_fmac_f32_e32 v123, v103, v2
	v_fmac_f32_e32 v124, v104, v2
	v_fmac_f32_e32 v125, v105, v2
	v_fmac_f32_e32 v126, v106, v2
	v_fmac_f32_e32 v127, v107, v2
	v_fmac_f32_e32 v128, v108, v2
	v_fmac_f32_e32 v129, v109, v2
	v_mov_b32_e32 v140, 0
	v_mov_b32_e32 v141, 0
	v_mov_b32_e32 v142, 0
	v_mov_b32_e32 v143, 0
	v_mov_b32_e32 v144, 0
	v_mov_b32_e32 v145, 0
	v_mov_b32_e32 v146, 0
	v_mov_b32_e32 v147, 0
	v_mov_b32_e32 v148, 0
	v_mov_b32_e32 v149, 0
	v_add_f32_dpp v120, v120, v120 row_ror:8 row_mask:0xf bank_mask:0xf bound_ctrl:1
	v_add_f32_dpp v121, v121, v121 row_ror:8 row_mask:0xf bank_mask:0xf bound_ctrl:1
	v_add_f32_dpp v122, v122, v122 row_ror:8 row_mask:0xf bank_mask:0xf bound_ctrl:1
	v_add_f32_dpp v123, v123, v123 row_ror:8 row_mask:0xf bank_mask:0xf bound_ctrl:1
	v_add_f32_dpp v124, v124, v124 row_ror:8 row_mask:0xf bank_mask:0xf bound_ctrl:1
	v_add_f32_dpp v125, v125, v125 row_ror:8 row_mask:0xf bank_mask:0xf bound_ctrl:1
	v_add_f32_dpp v126, v126, v126 row_ror:8 row_mask:0xf bank_mask:0xf bound_ctrl:1
	v_add_f32_dpp v127, v127, v127 row_ror:8 row_mask:0xf bank_mask:0xf bound_ctrl:1
	v_add_f32_dpp v128, v128, v128 row_ror:8 row_mask:0xf bank_mask:0xf bound_ctrl:1
	v_add_f32_dpp v129, v129, v129 row_ror:8 row_mask:0xf bank_mask:0xf bound_ctrl:1
	v_add_f32_dpp v120, v120, v120 row_ror:4 row_mask:0xf bank_mask:0xf bound_ctrl:1
	v_add_f32_dpp v121, v121, v121 row_ror:4 row_mask:0xf bank_mask:0xf bound_ctrl:1
	v_add_f32_dpp v122, v122, v122 row_ror:4 row_mask:0xf bank_mask:0xf bound_ctrl:1
	v_add_f32_dpp v123, v123, v123 row_ror:4 row_mask:0xf bank_mask:0xf bound_ctrl:1
	v_add_f32_dpp v124, v124, v124 row_ror:4 row_mask:0xf bank_mask:0xf bound_ctrl:1
	v_add_f32_dpp v125, v125, v125 row_ror:4 row_mask:0xf bank_mask:0xf bound_ctrl:1
	v_add_f32_dpp v126, v126, v126 row_ror:4 row_mask:0xf bank_mask:0xf bound_ctrl:1
	v_add_f32_dpp v127, v127, v127 row_ror:4 row_mask:0xf bank_mask:0xf bound_ctrl:1
	v_add_f32_dpp v128, v128, v128 row_ror:4 row_mask:0xf bank_mask:0xf bound_ctrl:1
	v_add_f32_dpp v129, v129, v129 row_ror:4 row_mask:0xf bank_mask:0xf bound_ctrl:1
	v_add_f32_dpp v120, v120, v120 row_ror:2 row_mask:0xf bank_mask:0xf bound_ctrl:1
	v_add_f32_dpp v121, v121, v121 row_ror:2 row_mask:0xf bank_mask:0xf bound_ctrl:1
	v_add_f32_dpp v122, v122, v122 row_ror:2 row_mask:0xf bank_mask:0xf bound_ctrl:1
	v_add_f32_dpp v123, v123, v123 row_ror:2 row_mask:0xf bank_mask:0xf bound_ctrl:1
	v_add_f32_dpp v124, v124, v124 row_ror:2 row_mask:0xf bank_mask:0xf bound_ctrl:1
	v_add_f32_dpp v125, v125, v125 row_ror:2 row_mask:0xf bank_mask:0xf bound_ctrl:1
	v_add_f32_dpp v126, v126, v126 row_ror:2 row_mask:0xf bank_mask:0xf bound_ctrl:1
	v_add_f32_dpp v127, v127, v127 row_ror:2 row_mask:0xf bank_mask:0xf bound_ctrl:1
	v_add_f32_dpp v128, v128, v128 row_ror:2 row_mask:0xf bank_mask:0xf bound_ctrl:1
	v_add_f32_dpp v129, v129, v129 row_ror:2 row_mask:0xf bank_mask:0xf bound_ctrl:1
	v_add_f32_dpp v120, v120, v120 row_ror:1 row_mask:0xf bank_mask:0xf bound_ctrl:1
	v_add_f32_dpp v121, v121, v121 row_ror:1 row_mask:0xf bank_mask:0xf bound_ctrl:1
	v_add_f32_dpp v122, v122, v122 row_ror:1 row_mask:0xf bank_mask:0xf bound_ctrl:1
	v_add_f32_dpp v123, v123, v123 row_ror:1 row_mask:0xf bank_mask:0xf bound_ctrl:1
	v_add_f32_dpp v124, v124, v124 row_ror:1 row_mask:0xf bank_mask:0xf bound_ctrl:1
	v_add_f32_dpp v125, v125, v125 row_ror:1 row_mask:0xf bank_mask:0xf bound_ctrl:1
	v_add_f32_dpp v126, v126, v126 row_ror:1 row_mask:0xf bank_mask:0xf bound_ctrl:1
	v_add_f32_dpp v127, v127, v127 row_ror:1 row_mask:0xf bank_mask:0xf bound_ctrl:1
	v_add_f32_dpp v128, v128, v128 row_ror:1 row_mask:0xf bank_mask:0xf bound_ctrl:1
	v_add_f32_dpp v129, v129, v129 row_ror:1 row_mask:0xf bank_mask:0xf bound_ctrl:1
	v_mov_b32_dpp v140, v120 row_bcast:15 row_mask:0xa bank_mask:0xf
	v_mov_b32_dpp v141, v121 row_bcast:15 row_mask:0xa bank_mask:0xf
	v_mov_b32_dpp v142, v122 row_bcast:15 row_mask:0xa bank_mask:0xf
	v_mov_b32_dpp v143, v123 row_bcast:15 row_mask:0xa bank_mask:0xf
	v_mov_b32_dpp v144, v124 row_bcast:15 row_mask:0xa bank_mask:0xf
	v_mov_b32_dpp v145, v125 row_bcast:15 row_mask:0xa bank_mask:0xf
	v_mov_b32_dpp v146, v126 row_bcast:15 row_mask:0xa bank_mask:0xf
	v_mov_b32_dpp v147, v127 row_bcast:15 row_mask:0xa bank_mask:0xf
	v_mov_b32_dpp v148, v128 row_bcast:15 row_mask:0xa bank_mask:0xf
	v_mov_b32_dpp v149, v129 row_bcast:15 row_mask:0xa bank_mask:0xf
	v_add_f32_e32 v120, v120, v140
	v_add_f32_e32 v121, v121, v141
	v_add_f32_e32 v122, v122, v142
	v_add_f32_e32 v123, v123, v143
	v_add_f32_e32 v124, v124, v144
	v_add_f32_e32 v125, v125, v145
	v_add_f32_e32 v126, v126, v146
	v_add_f32_e32 v127, v127, v147
	v_add_f32_e32 v128, v128, v148
	v_add_f32_e32 v129, v129, v149
	s_mov_b64 s[10:11], exec
	s_mov_b64 exec, s[6:7]
	ds_write_b32 v1, v120
	ds_write_b32 v1, v121 offset:32
	ds_write_b32 v1, v122 offset:64
	ds_write_b32 v1, v123 offset:96
	ds_write_b32 v1, v124 offset:128
	ds_write_b32 v1, v125 offset:160
	ds_write_b32 v1, v126 offset:192
	ds_write_b32 v1, v127 offset:224
	ds_write_b32 v1, v128 offset:256
	ds_write_b32 v1, v129 offset:288
	s_mov_b64 exec, s[10:11]
	s_cmpk_gt_u32 s2, 0x7f
	s_cbranch_scc1 .Lmy_ro_done
	v_mul_f32_e32 v130, v110, v4
	v_mul_f32_e32 v131, v111, v4
	v_mul_f32_e32 v132, v112, v4
	v_mul_f32_e32 v133, v113, v4
	v_mul_f32_e32 v134, v114, v4
	v_mul_f32_e32 v135, v115, v4
	v_mul_f32_e32 v136, v116, v4
	v_mul_f32_e32 v137, v117, v4
	v_mul_f32_e32 v138, v118, v4
	v_mul_f32_e32 v139, v119, v4
	v_fmac_f32_e32 v130, v100, v6
	v_fmac_f32_e32 v131, v101, v6
	v_fmac_f32_e32 v132, v102, v6
	v_fmac_f32_e32 v133, v103, v6
	v_fmac_f32_e32 v134, v104, v6
	v_fmac_f32_e32 v135, v105, v6
	v_fmac_f32_e32 v136, v106, v6
	v_fmac_f32_e32 v137, v107, v6
	v_fmac_f32_e32 v138, v108, v6
	v_fmac_f32_e32 v139, v109, v6
	v_mov_b32_e32 v140, 0
	v_mov_b32_e32 v141, 0
	v_mov_b32_e32 v142, 0
	v_mov_b32_e32 v143, 0
	v_mov_b32_e32 v144, 0
	v_mov_b32_e32 v145, 0
	v_mov_b32_e32 v146, 0
	v_mov_b32_e32 v147, 0
	v_mov_b32_e32 v148, 0
	v_mov_b32_e32 v149, 0
	v_add_f32_dpp v130, v130, v130 row_ror:8 row_mask:0xf bank_mask:0xf bound_ctrl:1
	v_add_f32_dpp v131, v131, v131 row_ror:8 row_mask:0xf bank_mask:0xf bound_ctrl:1
	v_add_f32_dpp v132, v132, v132 row_ror:8 row_mask:0xf bank_mask:0xf bound_ctrl:1
	v_add_f32_dpp v133, v133, v133 row_ror:8 row_mask:0xf bank_mask:0xf bound_ctrl:1
	v_add_f32_dpp v134, v134, v134 row_ror:8 row_mask:0xf bank_mask:0xf bound_ctrl:1
	v_add_f32_dpp v135, v135, v135 row_ror:8 row_mask:0xf bank_mask:0xf bound_ctrl:1
	v_add_f32_dpp v136, v136, v136 row_ror:8 row_mask:0xf bank_mask:0xf bound_ctrl:1
	v_add_f32_dpp v137, v137, v137 row_ror:8 row_mask:0xf bank_mask:0xf bound_ctrl:1
	v_add_f32_dpp v138, v138, v138 row_ror:8 row_mask:0xf bank_mask:0xf bound_ctrl:1
	v_add_f32_dpp v139, v139, v139 row_ror:8 row_mask:0xf bank_mask:0xf bound_ctrl:1
	v_add_f32_dpp v130, v130, v130 row_ror:4 row_mask:0xf bank_mask:0xf bound_ctrl:1
	v_add_f32_dpp v131, v131, v131 row_ror:4 row_mask:0xf bank_mask:0xf bound_ctrl:1
	v_add_f32_dpp v132, v132, v132 row_ror:4 row_mask:0xf bank_mask:0xf bound_ctrl:1
	v_add_f32_dpp v133, v133, v133 row_ror:4 row_mask:0xf bank_mask:0xf bound_ctrl:1
	v_add_f32_dpp v134, v134, v134 row_ror:4 row_mask:0xf bank_mask:0xf bound_ctrl:1
	v_add_f32_dpp v135, v135, v135 row_ror:4 row_mask:0xf bank_mask:0xf bound_ctrl:1
	v_add_f32_dpp v136, v136, v136 row_ror:4 row_mask:0xf bank_mask:0xf bound_ctrl:1
	v_add_f32_dpp v137, v137, v137 row_ror:4 row_mask:0xf bank_mask:0xf bound_ctrl:1
	v_add_f32_dpp v138, v138, v138 row_ror:4 row_mask:0xf bank_mask:0xf bound_ctrl:1
	v_add_f32_dpp v139, v139, v139 row_ror:4 row_mask:0xf bank_mask:0xf bound_ctrl:1
	v_add_f32_dpp v130, v130, v130 row_ror:2 row_mask:0xf bank_mask:0xf bound_ctrl:1
	v_add_f32_dpp v131, v131, v131 row_ror:2 row_mask:0xf bank_mask:0xf bound_ctrl:1
	v_add_f32_dpp v132, v132, v132 row_ror:2 row_mask:0xf bank_mask:0xf bound_ctrl:1
	v_add_f32_dpp v133, v133, v133 row_ror:2 row_mask:0xf bank_mask:0xf bound_ctrl:1
	v_add_f32_dpp v134, v134, v134 row_ror:2 row_mask:0xf bank_mask:0xf bound_ctrl:1
	v_add_f32_dpp v135, v135, v135 row_ror:2 row_mask:0xf bank_mask:0xf bound_ctrl:1
	v_add_f32_dpp v136, v136, v136 row_ror:2 row_mask:0xf bank_mask:0xf bound_ctrl:1
	v_add_f32_dpp v137, v137, v137 row_ror:2 row_mask:0xf bank_mask:0xf bound_ctrl:1
	v_add_f32_dpp v138, v138, v138 row_ror:2 row_mask:0xf bank_mask:0xf bound_ctrl:1
	v_add_f32_dpp v139, v139, v139 row_ror:2 row_mask:0xf bank_mask:0xf bound_ctrl:1
	v_add_f32_dpp v130, v130, v130 row_ror:1 row_mask:0xf bank_mask:0xf bound_ctrl:1
	v_add_f32_dpp v131, v131, v131 row_ror:1 row_mask:0xf bank_mask:0xf bound_ctrl:1
	v_add_f32_dpp v132, v132, v132 row_ror:1 row_mask:0xf bank_mask:0xf bound_ctrl:1
	v_add_f32_dpp v133, v133, v133 row_ror:1 row_mask:0xf bank_mask:0xf bound_ctrl:1
	v_add_f32_dpp v134, v134, v134 row_ror:1 row_mask:0xf bank_mask:0xf bound_ctrl:1
	v_add_f32_dpp v135, v135, v135 row_ror:1 row_mask:0xf bank_mask:0xf bound_ctrl:1
	v_add_f32_dpp v136, v136, v136 row_ror:1 row_mask:0xf bank_mask:0xf bound_ctrl:1
	v_add_f32_dpp v137, v137, v137 row_ror:1 row_mask:0xf bank_mask:0xf bound_ctrl:1
	v_add_f32_dpp v138, v138, v138 row_ror:1 row_mask:0xf bank_mask:0xf bound_ctrl:1
	v_add_f32_dpp v139, v139, v139 row_ror:1 row_mask:0xf bank_mask:0xf bound_ctrl:1
	v_mov_b32_dpp v140, v130 row_bcast:15 row_mask:0xa bank_mask:0xf
	v_mov_b32_dpp v141, v131 row_bcast:15 row_mask:0xa bank_mask:0xf
	v_mov_b32_dpp v142, v132 row_bcast:15 row_mask:0xa bank_mask:0xf
	v_mov_b32_dpp v143, v133 row_bcast:15 row_mask:0xa bank_mask:0xf
	v_mov_b32_dpp v144, v134 row_bcast:15 row_mask:0xa bank_mask:0xf
	v_mov_b32_dpp v145, v135 row_bcast:15 row_mask:0xa bank_mask:0xf
	v_mov_b32_dpp v146, v136 row_bcast:15 row_mask:0xa bank_mask:0xf
	v_mov_b32_dpp v147, v137 row_bcast:15 row_mask:0xa bank_mask:0xf
	v_mov_b32_dpp v148, v138 row_bcast:15 row_mask:0xa bank_mask:0xf
	v_mov_b32_dpp v149, v139 row_bcast:15 row_mask:0xa bank_mask:0xf
	v_add_f32_e32 v130, v130, v140
	v_add_f32_e32 v131, v131, v141
	v_add_f32_e32 v132, v132, v142
	v_add_f32_e32 v133, v133, v143
	v_add_f32_e32 v134, v134, v144
	v_add_f32_e32 v135, v135, v145
	v_add_f32_e32 v136, v136, v146
	v_add_f32_e32 v137, v137, v147
	v_add_f32_e32 v138, v138, v148
	v_add_f32_e32 v139, v139, v149
	s_mov_b64 exec, s[6:7]
	ds_write_b32 v1, v130 offset:320
	ds_write_b32 v1, v131 offset:352
	ds_write_b32 v1, v132 offset:384
	ds_write_b32 v1, v133 offset:416
	ds_write_b32 v1, v134 offset:448
	ds_write_b32 v1, v135 offset:480
	ds_write_b32 v1, v136 offset:512
	ds_write_b32 v1, v137 offset:544
	ds_write_b32 v1, v138 offset:576
	ds_write_b32 v1, v139 offset:608
	s_mov_b64 exec, s[10:11]
.Lmy_ro_done:
.Lk_388:
	s_or_b64 exec, exec, s[4:5]
	s_add_i32 s2, s33, 32
	v_mov_b32_e32 v0, s2
	v_mov_b32_e32 v1, s33
	v_cmp_gt_u32_e32 vcc, 10, v98
	v_cmp_gt_u32_e64 s[0:1], 20, v98
	s_waitcnt lgkmcnt(0)
	v_cndmask_b32_e32 v0, v0, v1, vcc
	v_cmp_gt_u32_e64 s[2:3], 48, v0
	s_and_b64 s[0:1], s[0:1], s[2:3]
	s_barrier
	s_and_saveexec_b64 s[2:3], s[0:1]
	s_cbranch_execz .Lk_390
	v_mov_b32_e32 v1, 0x25000
	v_lshl_add_u32 v1, v98, 5, v1
	ds_read_b128 v[2:5], v1
	v_add_u32_e32 v6, -10, v98
	v_cndmask_b32_e32 v12, v6, v98, vcc
	ds_read_b128 v[6:9], v1 offset:16
	v_add_u32_e32 v0, s74, v0
	s_waitcnt lgkmcnt(1)
	v_add_f32_e32 v1, 0, v2
	v_add_f32_e32 v1, v1, v3
	v_add_f32_e32 v1, v1, v4
	v_add_f32_e32 v1, v1, v5
	s_waitcnt lgkmcnt(0)
	v_add_f32_e32 v1, v1, v6
	v_add_f32_e32 v1, v1, v7
	v_add_f32_e32 v1, v1, v8
	v_mov_b32_e32 v10, s64
	v_mov_b32_e32 v11, s65
	v_add_f32_e32 v2, v1, v9
	v_mul_lo_u32 v0, v0, 10
	v_mov_b32_e32 v1, 0
	v_mov_b32_e32 v13, v1
	v_lshl_add_u64 v[0:1], v[0:1], 2, v[10:11]
	v_lshl_add_u64 v[0:1], v[12:13], 2, v[0:1]
	global_store_dword v[0:1], v2, off
